# GEMM loop: LDS-DMA issue spread (3 A pieces after the barrier, 3 B pieces in the next pre-barrier MFMA block, one per 6 MFMAs)
# speedup vs baseline: 1.0952x; 1.0135x over previous
_Z8gemm_qkvPKDF16_S0_PKfPDF16_S3_S3_Pj:
	v_readfirstlane_b32 s13, v0
	s_lshr_b32 s8, s13, 6
	v_bfe_u32 v2, v0, 3, 3
	s_load_dwordx4 s[4:7], s[0:1], 0x0
	v_lshl_or_b32 v6, s8, 3, v2
	v_lshrrev_b32_e32 v2, 1, v6
	s_mul_i32 s16, s3, 0xc0
	v_xor_b32_e32 v4, v2, v0
	v_add_u32_e32 v2, s16, v6
	v_ashrrev_i32_e32 v3, 31, v2
	s_bfe_u32 s15, s13, 0x20006
	v_lshlrev_b64 v[2:3], 11, v[2:3]
	v_lshlrev_b32_e32 v4, 4, v4
	s_mul_i32 s10, s2, 0xc0
	s_mul_i32 s2, s15, 48
	s_waitcnt lgkmcnt(0)
	v_lshl_add_u64 v[2:3], s[4:5], 0, v[2:3]
	v_and_b32_e32 v4, 0x70, v4
	v_mov_b32_e32 v5, 0
	s_add_i32 s17, s2, s10
	v_lshl_add_u64 v[218:219], v[2:3], 0, v[4:5]
	v_add_u32_e32 v2, s10, v6
	s_lshl_b32 s8, s8, 10
	v_ashrrev_i32_e32 v3, 31, v2
	s_cmp_lg_u32 0x400, -1
	v_lshlrev_b64 v[2:3], 11, v[2:3]
	s_cselect_b32 s4, 0x400, 0
	v_lshl_add_u64 v[2:3], s[6:7], 0, v[2:3]
	s_add_i32 s11, s8, s4
	s_mov_b32 s4, m0
	s_mov_b32 m0, s11
	s_nop 0
	global_load_lds_dwordx4 v[218:219], off
	s_mov_b32 m0, s4
	v_lshl_add_u64 v[220:221], v[2:3], 0, v[4:5]
	s_add_i32 s4, s11, 0x6000
	s_mov_b32 s5, m0
	s_mov_b32 m0, s4
	s_nop 0
	global_load_lds_dwordx4 v[220:221], off
	s_mov_b32 m0, s5
	s_mov_b64 s[4:5], 0x20000
	v_lshl_add_u64 v[222:223], v[218:219], 0, s[4:5]
	s_add_i32 s9, s11, 0x2000
	s_mov_b32 s6, m0
	s_mov_b32 m0, s9
	s_nop 0
	global_load_lds_dwordx4 v[222:223], off
	s_mov_b32 m0, s6
	v_lshl_add_u64 v[224:225], v[220:221], 0, s[4:5]
	s_add_i32 s4, s11, 0x8000
	s_mov_b32 s5, m0
	s_mov_b32 m0, s4
	s_nop 0
	global_load_lds_dwordx4 v[224:225], off
	s_mov_b32 m0, s5
	s_mov_b64 s[4:5], 0x40000
	v_lshl_add_u64 v[226:227], v[218:219], 0, s[4:5]
	s_add_i32 s12, s11, 0x4000
	s_mov_b32 s6, m0
	s_mov_b32 m0, s12
	s_nop 0
	global_load_lds_dwordx4 v[226:227], off
	s_mov_b32 m0, s6
	v_lshl_add_u64 v[228:229], v[220:221], 0, s[4:5]
	s_add_i32 s4, s11, 0xa000
	s_mov_b32 s5, m0
	s_mov_b32 m0, s4
	s_nop 0
	global_load_lds_dwordx4 v[228:229], off
	s_mov_b32 m0, s5
	s_cmpk_gt_i32 s17, 0x7d0
	s_cselect_b64 s[4:5], -1, 0
	s_lshr_b32 s14, s13, 8
	s_mul_i32 s6, s14, 0x3000
	s_add_i32 s13, s6, 0x400
	s_mov_b64 s[6:7], 0x80
	s_add_i32 s18, s11, 0xc000
	v_lshl_add_u64 v[2:3], v[218:219], 0, s[6:7]
	s_mov_b32 s30, m0
	s_mov_b32 m0, s18
	s_nop 0
	global_load_lds_dwordx4 v[2:3], off
	s_mov_b32 m0, s30
	s_add_i32 s19, s11, 0x12000
	v_lshl_add_u64 v[2:3], v[220:221], 0, s[6:7]
	s_mov_b32 s6, m0
	s_mov_b32 m0, s19
	s_nop 0
	global_load_lds_dwordx4 v[2:3], off
	s_mov_b32 m0, s6
	s_mov_b64 s[6:7], 0x20080
	s_add_i32 s20, s11, 0xe000
	v_lshl_add_u64 v[2:3], v[218:219], 0, s[6:7]
	s_mov_b32 s18, m0
	s_mov_b32 m0, s20
	s_nop 0
	global_load_lds_dwordx4 v[2:3], off
	s_mov_b32 m0, s18
	s_add_i32 s21, s11, 0x14000
	v_lshl_add_u64 v[2:3], v[220:221], 0, s[6:7]
	s_mov_b32 s6, m0
	s_mov_b32 m0, s21
	s_nop 0
	global_load_lds_dwordx4 v[2:3], off
	s_mov_b32 m0, s6
	s_mov_b64 s[6:7], 0x40080
	v_lshl_add_u64 v[2:3], v[218:219], 0, s[6:7]
	s_add_i32 s22, s11, 0x10000
	s_mov_b32 s18, m0
	s_mov_b32 m0, s22
	s_nop 0
	global_load_lds_dwordx4 v[2:3], off
	s_mov_b32 m0, s18
	v_lshl_add_u64 v[2:3], v[220:221], 0, s[6:7]
	v_and_b32_e32 v1, 15, v0
	v_bfe_u32 v231, v0, 4, 2
	s_add_i32 s23, s11, 0x16000
	s_mov_b32 s6, m0
	s_mov_b32 m0, s23
	s_nop 0
	global_load_lds_dwordx4 v[2:3], off
	s_mov_b32 m0, s6
	v_lshrrev_b32_e32 v3, 1, v0
	v_lshlrev_b32_e32 v2, 7, v1
	v_bfe_u32 v4, v0, 1, 3
	v_bitop3_b32 v3, v231, v3, 7 bitop3:0x78
	v_lshl_or_b32 v238, v3, 4, v2
	v_bitop3_b32 v3, v231, v4, 4 bitop3:0x36
	v_lshl_or_b32 v240, v3, 4, v2
	s_mulk_i32 s15, 0x1800
	s_addk_i32 s15, 0x6400
	v_add_u32_e32 v158, s13, v238
	v_add_u32_e32 v160, s13, v240
	v_add_u32_e32 v162, s15, v238
	v_add_u32_e32 v164, s15, v240
	s_add_u32 m0, s11, 0x17f00
	s_nop 0
	global_load_lds_dwordx4 v[218:219], off offset:256
	s_add_u32 m0, s11, 0x19f00
	s_nop 0
	global_load_lds_dwordx4 v[222:223], off offset:256
	s_add_u32 m0, s11, 0x1bf00
	s_nop 0
	global_load_lds_dwordx4 v[226:227], off offset:256
	s_load_dwordx2 s[24:25], s[0:1], 0x10
	s_mov_b32 s20, 0x180
	s_mov_b32 s21, 0
	v_lshl_add_u64 v[218:219], v[218:219], 0, s[20:21]
	v_lshl_add_u64 v[222:223], v[222:223], 0, s[20:21]
	v_lshl_add_u64 v[226:227], v[226:227], 0, s[20:21]
	v_lshl_add_u64 v[220:221], v[220:221], 0, s[20:21]
	v_lshl_add_u64 v[224:225], v[224:225], 0, s[20:21]
	v_lshl_add_u64 v[228:229], v[228:229], 0, s[20:21]
	v_add_u32_e32 v159, 0x18000, v158
	v_add_u32_e32 v161, 0x18000, v160
	v_add_u32_e32 v163, 0x18000, v162
	v_add_u32_e32 v165, 0x18000, v164
	v_mov_b32_e32 v82, 0
	v_mov_b32_e32 v83, 0
	v_mov_b32_e32 v84, 0
	v_mov_b32_e32 v85, 0
	v_mov_b32_e32 v58, 0
	v_mov_b32_e32 v59, 0
	v_mov_b32_e32 v60, 0
	v_mov_b32_e32 v61, 0
	v_mov_b32_e32 v14, 0
	v_mov_b32_e32 v15, 0
	v_mov_b32_e32 v16, 0
	v_mov_b32_e32 v17, 0
	v_mov_b32_e32 v78, 0
	v_mov_b32_e32 v79, 0
	v_mov_b32_e32 v80, 0
	v_mov_b32_e32 v81, 0
	v_mov_b32_e32 v22, 0
	v_mov_b32_e32 v23, 0
	v_mov_b32_e32 v24, 0
	v_mov_b32_e32 v25, 0
	v_mov_b32_e32 v30, 0
	v_mov_b32_e32 v31, 0
	v_mov_b32_e32 v32, 0
	v_mov_b32_e32 v33, 0
	v_mov_b32_e32 v74, 0
	v_mov_b32_e32 v75, 0
	v_mov_b32_e32 v76, 0
	v_mov_b32_e32 v77, 0
	v_mov_b32_e32 v18, 0
	v_mov_b32_e32 v19, 0
	v_mov_b32_e32 v20, 0
	v_mov_b32_e32 v21, 0
	v_mov_b32_e32 v26, 0
	v_mov_b32_e32 v27, 0
	v_mov_b32_e32 v28, 0
	v_mov_b32_e32 v29, 0
	v_mov_b32_e32 v70, 0
	v_mov_b32_e32 v71, 0
	v_mov_b32_e32 v72, 0
	v_mov_b32_e32 v73, 0
	v_mov_b32_e32 v46, 0
	v_mov_b32_e32 v47, 0
	v_mov_b32_e32 v48, 0
	v_mov_b32_e32 v49, 0
	v_mov_b32_e32 v240, 0
	v_mov_b32_e32 v241, 0
	v_mov_b32_e32 v242, 0
	v_mov_b32_e32 v243, 0
	v_mov_b32_e32 v66, 0
	v_mov_b32_e32 v67, 0
	v_mov_b32_e32 v68, 0
	v_mov_b32_e32 v69, 0
	v_mov_b32_e32 v42, 0
	v_mov_b32_e32 v43, 0
	v_mov_b32_e32 v44, 0
	v_mov_b32_e32 v45, 0
	v_mov_b32_e32 v236, 0
	v_mov_b32_e32 v237, 0
	v_mov_b32_e32 v238, 0
	v_mov_b32_e32 v239, 0
	v_mov_b32_e32 v62, 0
	v_mov_b32_e32 v63, 0
	v_mov_b32_e32 v64, 0
	v_mov_b32_e32 v65, 0
	v_mov_b32_e32 v38, 0
	v_mov_b32_e32 v39, 0
	v_mov_b32_e32 v40, 0
	v_mov_b32_e32 v41, 0
	v_mov_b32_e32 v34, 0
	v_mov_b32_e32 v35, 0
	v_mov_b32_e32 v36, 0
	v_mov_b32_e32 v37, 0
	s_not_b64 s[6:7], s[4:5]
	s_mov_b32 s22, 4
	s_waitcnt vmcnt(9) lgkmcnt(0)
	s_barrier
	ds_read_b128 v[134:137], v162
	ds_read_b128 v[138:141], v162 offset:2048
	ds_read_b128 v[142:145], v162 offset:4096
	ds_read_b128 v[86:89], v158
	ds_read_b128 v[90:93], v158 offset:2048
	ds_read_b128 v[94:97], v158 offset:4096
	ds_read_b128 v[98:101], v158 offset:6144
	ds_read_b128 v[102:105], v158 offset:8192
	ds_read_b128 v[106:109], v158 offset:10240
	ds_read_b128 v[110:113], v160
	ds_read_b128 v[114:117], v160 offset:2048
	ds_read_b128 v[118:121], v160 offset:4096
	ds_read_b128 v[122:125], v160 offset:6144
	ds_read_b128 v[126:129], v160 offset:8192
	ds_read_b128 v[130:133], v160 offset:10240
	ds_read_b128 v[146:149], v164
	ds_read_b128 v[150:153], v164 offset:2048
	ds_read_b128 v[154:157], v164 offset:4096
	s_and_b64 vcc, exec, s[4:5]
	s_cbranch_vccnz .Lgemm_N_loop
.Lgemm_T_loop:
	s_waitcnt lgkmcnt(9)
	s_add_u32 m0, s11, 0x1e080
	v_mfma_f32_16x16x32_f16 v[82:85], v[134:137], v[86:89], v[82:85]
	global_load_lds_dwordx4 v[220:221], off offset:-128
	v_mfma_f32_16x16x32_f16 v[58:61], v[138:141], v[86:89], v[58:61]
	v_mfma_f32_16x16x32_f16 v[14:17], v[142:145], v[86:89], v[14:17]
	v_mfma_f32_16x16x32_f16 v[78:81], v[134:137], v[90:93], v[78:81]
	v_mfma_f32_16x16x32_f16 v[22:25], v[138:141], v[90:93], v[22:25]
	v_mfma_f32_16x16x32_f16 v[30:33], v[142:145], v[90:93], v[30:33]
	s_add_u32 m0, s11, 0x20080
	v_mfma_f32_16x16x32_f16 v[74:77], v[134:137], v[94:97], v[74:77]
	global_load_lds_dwordx4 v[224:225], off offset:-128
	v_mfma_f32_16x16x32_f16 v[18:21], v[138:141], v[94:97], v[18:21]
	v_mfma_f32_16x16x32_f16 v[26:29], v[142:145], v[94:97], v[26:29]
	v_mfma_f32_16x16x32_f16 v[70:73], v[134:137], v[98:101], v[70:73]
	v_mfma_f32_16x16x32_f16 v[46:49], v[138:141], v[98:101], v[46:49]
	v_mfma_f32_16x16x32_f16 v[240:243], v[142:145], v[98:101], v[240:243]
	s_add_u32 m0, s11, 0x22080
	v_mfma_f32_16x16x32_f16 v[66:69], v[134:137], v[102:105], v[66:69]
	global_load_lds_dwordx4 v[228:229], off offset:-128
	v_mfma_f32_16x16x32_f16 v[42:45], v[138:141], v[102:105], v[42:45]
	v_mfma_f32_16x16x32_f16 v[236:239], v[142:145], v[102:105], v[236:239]
	v_mfma_f32_16x16x32_f16 v[62:65], v[134:137], v[106:109], v[62:65]
	v_mfma_f32_16x16x32_f16 v[38:41], v[138:141], v[106:109], v[38:41]
	v_mfma_f32_16x16x32_f16 v[34:37], v[142:145], v[106:109], v[34:37]
	s_waitcnt vmcnt(6) lgkmcnt(0)
	s_barrier
	s_add_u32 m0, s11, 0x0
	ds_read_b128 v[134:137], v162 offset:49152
	global_load_lds_dwordx4 v[218:219], off
	v_mfma_f32_16x16x32_f16 v[82:85], v[146:149], v[110:113], v[82:85]
	ds_read_b128 v[138:141], v162 offset:51200
	v_mfma_f32_16x16x32_f16 v[58:61], v[150:153], v[110:113], v[58:61]
	ds_read_b128 v[142:145], v162 offset:53248
	v_mfma_f32_16x16x32_f16 v[14:17], v[154:157], v[110:113], v[14:17]
	ds_read_b128 v[86:89], v158 offset:49152
	v_mfma_f32_16x16x32_f16 v[78:81], v[146:149], v[114:117], v[78:81]
	ds_read_b128 v[90:93], v158 offset:51200
	v_mfma_f32_16x16x32_f16 v[22:25], v[150:153], v[114:117], v[22:25]
	ds_read_b128 v[94:97], v158 offset:53248
	v_mfma_f32_16x16x32_f16 v[30:33], v[154:157], v[114:117], v[30:33]
	s_add_u32 m0, s11, 0x2000
	ds_read_b128 v[98:101], v158 offset:55296
	global_load_lds_dwordx4 v[222:223], off
	v_mfma_f32_16x16x32_f16 v[74:77], v[146:149], v[118:121], v[74:77]
	ds_read_b128 v[102:105], v158 offset:57344
	v_mfma_f32_16x16x32_f16 v[18:21], v[150:153], v[118:121], v[18:21]
	ds_read_b128 v[106:109], v158 offset:59392
	v_mfma_f32_16x16x32_f16 v[26:29], v[154:157], v[118:121], v[26:29]
	ds_read_b128 v[110:113], v160 offset:49152
	v_mfma_f32_16x16x32_f16 v[70:73], v[146:149], v[122:125], v[70:73]
	ds_read_b128 v[114:117], v160 offset:51200
	v_mfma_f32_16x16x32_f16 v[46:49], v[150:153], v[122:125], v[46:49]
	v_mfma_f32_16x16x32_f16 v[240:243], v[154:157], v[122:125], v[240:243]
	s_add_u32 m0, s11, 0x4000
	ds_read_b128 v[118:121], v160 offset:53248
	global_load_lds_dwordx4 v[226:227], off
	v_mfma_f32_16x16x32_f16 v[66:69], v[146:149], v[126:129], v[66:69]
	ds_read_b128 v[122:125], v160 offset:55296
	v_mfma_f32_16x16x32_f16 v[42:45], v[150:153], v[126:129], v[42:45]
	v_mfma_f32_16x16x32_f16 v[236:239], v[154:157], v[126:129], v[236:239]
	ds_read_b128 v[126:129], v160 offset:57344
	v_mfma_f32_16x16x32_f16 v[62:65], v[146:149], v[130:133], v[62:65]
	v_mfma_f32_16x16x32_f16 v[38:41], v[150:153], v[130:133], v[38:41]
	v_mfma_f32_16x16x32_f16 v[34:37], v[154:157], v[130:133], v[34:37]
	ds_read_b128 v[130:133], v160 offset:59392
	ds_read_b128 v[146:149], v164 offset:49152
	ds_read_b128 v[150:153], v164 offset:51200
	ds_read_b128 v[154:157], v164 offset:53248
	s_waitcnt lgkmcnt(9)
	s_add_u32 m0, s11, 0x6000
	v_mfma_f32_16x16x32_f16 v[82:85], v[134:137], v[86:89], v[82:85]
	global_load_lds_dwordx4 v[220:221], off
	v_mfma_f32_16x16x32_f16 v[58:61], v[138:141], v[86:89], v[58:61]
	v_mfma_f32_16x16x32_f16 v[14:17], v[142:145], v[86:89], v[14:17]
	v_mfma_f32_16x16x32_f16 v[78:81], v[134:137], v[90:93], v[78:81]
	v_mfma_f32_16x16x32_f16 v[22:25], v[138:141], v[90:93], v[22:25]
	v_mfma_f32_16x16x32_f16 v[30:33], v[142:145], v[90:93], v[30:33]
	s_add_u32 m0, s11, 0x8000
	v_mfma_f32_16x16x32_f16 v[74:77], v[134:137], v[94:97], v[74:77]
	global_load_lds_dwordx4 v[224:225], off
	v_mfma_f32_16x16x32_f16 v[18:21], v[138:141], v[94:97], v[18:21]
	v_mfma_f32_16x16x32_f16 v[26:29], v[142:145], v[94:97], v[26:29]
	v_mfma_f32_16x16x32_f16 v[70:73], v[134:137], v[98:101], v[70:73]
	v_mfma_f32_16x16x32_f16 v[46:49], v[138:141], v[98:101], v[46:49]
	v_mfma_f32_16x16x32_f16 v[240:243], v[142:145], v[98:101], v[240:243]
	s_add_u32 m0, s11, 0xa000
	v_mfma_f32_16x16x32_f16 v[66:69], v[134:137], v[102:105], v[66:69]
	global_load_lds_dwordx4 v[228:229], off
	v_mfma_f32_16x16x32_f16 v[42:45], v[138:141], v[102:105], v[42:45]
	v_mfma_f32_16x16x32_f16 v[236:239], v[142:145], v[102:105], v[236:239]
	v_mfma_f32_16x16x32_f16 v[62:65], v[134:137], v[106:109], v[62:65]
	v_mfma_f32_16x16x32_f16 v[38:41], v[138:141], v[106:109], v[38:41]
	v_mfma_f32_16x16x32_f16 v[34:37], v[142:145], v[106:109], v[34:37]
	s_waitcnt vmcnt(6) lgkmcnt(0)
	s_barrier
	s_add_u32 m0, s11, 0xbf80
	ds_read_b128 v[134:137], v163
	global_load_lds_dwordx4 v[218:219], off offset:128
	v_mfma_f32_16x16x32_f16 v[82:85], v[146:149], v[110:113], v[82:85]
	ds_read_b128 v[138:141], v163 offset:2048
	v_mfma_f32_16x16x32_f16 v[58:61], v[150:153], v[110:113], v[58:61]
	ds_read_b128 v[142:145], v163 offset:4096
	v_mfma_f32_16x16x32_f16 v[14:17], v[154:157], v[110:113], v[14:17]
	ds_read_b128 v[86:89], v159
	v_mfma_f32_16x16x32_f16 v[78:81], v[146:149], v[114:117], v[78:81]
	ds_read_b128 v[90:93], v159 offset:2048
	v_mfma_f32_16x16x32_f16 v[22:25], v[150:153], v[114:117], v[22:25]
	ds_read_b128 v[94:97], v159 offset:4096
	v_mfma_f32_16x16x32_f16 v[30:33], v[154:157], v[114:117], v[30:33]
	s_add_u32 m0, s11, 0xdf80
	ds_read_b128 v[98:101], v159 offset:6144
	global_load_lds_dwordx4 v[222:223], off offset:128
	v_mfma_f32_16x16x32_f16 v[74:77], v[146:149], v[118:121], v[74:77]
	ds_read_b128 v[102:105], v159 offset:8192
	v_mfma_f32_16x16x32_f16 v[18:21], v[150:153], v[118:121], v[18:21]
	ds_read_b128 v[106:109], v159 offset:10240
	v_mfma_f32_16x16x32_f16 v[26:29], v[154:157], v[118:121], v[26:29]
	ds_read_b128 v[110:113], v161
	v_mfma_f32_16x16x32_f16 v[70:73], v[146:149], v[122:125], v[70:73]
	ds_read_b128 v[114:117], v161 offset:2048
	v_mfma_f32_16x16x32_f16 v[46:49], v[150:153], v[122:125], v[46:49]
	v_mfma_f32_16x16x32_f16 v[240:243], v[154:157], v[122:125], v[240:243]
	s_add_u32 m0, s11, 0xff80
	ds_read_b128 v[118:121], v161 offset:4096
	global_load_lds_dwordx4 v[226:227], off offset:128
	v_mfma_f32_16x16x32_f16 v[66:69], v[146:149], v[126:129], v[66:69]
	ds_read_b128 v[122:125], v161 offset:6144
	v_mfma_f32_16x16x32_f16 v[42:45], v[150:153], v[126:129], v[42:45]
	v_mfma_f32_16x16x32_f16 v[236:239], v[154:157], v[126:129], v[236:239]
	ds_read_b128 v[126:129], v161 offset:8192
	v_mfma_f32_16x16x32_f16 v[62:65], v[146:149], v[130:133], v[62:65]
	v_mfma_f32_16x16x32_f16 v[38:41], v[150:153], v[130:133], v[38:41]
	v_mfma_f32_16x16x32_f16 v[34:37], v[154:157], v[130:133], v[34:37]
	ds_read_b128 v[130:133], v161 offset:10240
	ds_read_b128 v[146:149], v165
	ds_read_b128 v[150:153], v165 offset:2048
	ds_read_b128 v[154:157], v165 offset:4096
	s_waitcnt lgkmcnt(9)
	s_add_u32 m0, s11, 0x11f80
	v_mfma_f32_16x16x32_f16 v[82:85], v[134:137], v[86:89], v[82:85]
	global_load_lds_dwordx4 v[220:221], off offset:128
	v_mfma_f32_16x16x32_f16 v[58:61], v[138:141], v[86:89], v[58:61]
	v_mfma_f32_16x16x32_f16 v[14:17], v[142:145], v[86:89], v[14:17]
	v_mfma_f32_16x16x32_f16 v[78:81], v[134:137], v[90:93], v[78:81]
	v_mfma_f32_16x16x32_f16 v[22:25], v[138:141], v[90:93], v[22:25]
	v_mfma_f32_16x16x32_f16 v[30:33], v[142:145], v[90:93], v[30:33]
	s_add_u32 m0, s11, 0x13f80
	v_mfma_f32_16x16x32_f16 v[74:77], v[134:137], v[94:97], v[74:77]
	global_load_lds_dwordx4 v[224:225], off offset:128
	v_mfma_f32_16x16x32_f16 v[18:21], v[138:141], v[94:97], v[18:21]
	v_mfma_f32_16x16x32_f16 v[26:29], v[142:145], v[94:97], v[26:29]
	v_mfma_f32_16x16x32_f16 v[70:73], v[134:137], v[98:101], v[70:73]
	v_mfma_f32_16x16x32_f16 v[46:49], v[138:141], v[98:101], v[46:49]
	v_mfma_f32_16x16x32_f16 v[240:243], v[142:145], v[98:101], v[240:243]
	s_add_u32 m0, s11, 0x15f80
	v_mfma_f32_16x16x32_f16 v[66:69], v[134:137], v[102:105], v[66:69]
	global_load_lds_dwordx4 v[228:229], off offset:128
	v_mfma_f32_16x16x32_f16 v[42:45], v[138:141], v[102:105], v[42:45]
	v_mfma_f32_16x16x32_f16 v[236:239], v[142:145], v[102:105], v[236:239]
	v_mfma_f32_16x16x32_f16 v[62:65], v[134:137], v[106:109], v[62:65]
	v_mfma_f32_16x16x32_f16 v[38:41], v[138:141], v[106:109], v[38:41]
	v_mfma_f32_16x16x32_f16 v[34:37], v[142:145], v[106:109], v[34:37]
	s_waitcnt vmcnt(6) lgkmcnt(0)
	s_barrier
	s_add_u32 m0, s11, 0x17f00
	ds_read_b128 v[134:137], v162
	global_load_lds_dwordx4 v[218:219], off offset:256
	v_mfma_f32_16x16x32_f16 v[82:85], v[146:149], v[110:113], v[82:85]
	ds_read_b128 v[138:141], v162 offset:2048
	v_mfma_f32_16x16x32_f16 v[58:61], v[150:153], v[110:113], v[58:61]
	ds_read_b128 v[142:145], v162 offset:4096
	v_mfma_f32_16x16x32_f16 v[14:17], v[154:157], v[110:113], v[14:17]
	ds_read_b128 v[86:89], v158
	v_mfma_f32_16x16x32_f16 v[78:81], v[146:149], v[114:117], v[78:81]
	ds_read_b128 v[90:93], v158 offset:2048
	v_mfma_f32_16x16x32_f16 v[22:25], v[150:153], v[114:117], v[22:25]
	ds_read_b128 v[94:97], v158 offset:4096
	v_mfma_f32_16x16x32_f16 v[30:33], v[154:157], v[114:117], v[30:33]
	s_add_u32 m0, s11, 0x19f00
	ds_read_b128 v[98:101], v158 offset:6144
	global_load_lds_dwordx4 v[222:223], off offset:256
	v_mfma_f32_16x16x32_f16 v[74:77], v[146:149], v[118:121], v[74:77]
	ds_read_b128 v[102:105], v158 offset:8192
	v_mfma_f32_16x16x32_f16 v[18:21], v[150:153], v[118:121], v[18:21]
	ds_read_b128 v[106:109], v158 offset:10240
	v_mfma_f32_16x16x32_f16 v[26:29], v[154:157], v[118:121], v[26:29]
	ds_read_b128 v[110:113], v160
	v_mfma_f32_16x16x32_f16 v[70:73], v[146:149], v[122:125], v[70:73]
	ds_read_b128 v[114:117], v160 offset:2048
	v_mfma_f32_16x16x32_f16 v[46:49], v[150:153], v[122:125], v[46:49]
	v_mfma_f32_16x16x32_f16 v[240:243], v[154:157], v[122:125], v[240:243]
	s_add_u32 m0, s11, 0x1bf00
	ds_read_b128 v[118:121], v160 offset:4096
	global_load_lds_dwordx4 v[226:227], off offset:256
	v_mfma_f32_16x16x32_f16 v[66:69], v[146:149], v[126:129], v[66:69]
	ds_read_b128 v[122:125], v160 offset:6144
	v_mfma_f32_16x16x32_f16 v[42:45], v[150:153], v[126:129], v[42:45]
	v_mfma_f32_16x16x32_f16 v[236:239], v[154:157], v[126:129], v[236:239]
	ds_read_b128 v[126:129], v160 offset:8192
	v_mfma_f32_16x16x32_f16 v[62:65], v[146:149], v[130:133], v[62:65]
	v_mfma_f32_16x16x32_f16 v[38:41], v[150:153], v[130:133], v[38:41]
	v_mfma_f32_16x16x32_f16 v[34:37], v[154:157], v[130:133], v[34:37]
	ds_read_b128 v[130:133], v160 offset:10240
	ds_read_b128 v[146:149], v164
	ds_read_b128 v[150:153], v164 offset:2048
	ds_read_b128 v[154:157], v164 offset:4096
	v_lshl_add_u64 v[218:219], v[218:219], 0, s[20:21]
	v_lshl_add_u64 v[222:223], v[222:223], 0, s[20:21]
	v_lshl_add_u64 v[226:227], v[226:227], 0, s[20:21]
	v_lshl_add_u64 v[220:221], v[220:221], 0, s[20:21]
	v_lshl_add_u64 v[224:225], v[224:225], 0, s[20:21]
	v_lshl_add_u64 v[228:229], v[228:229], 0, s[20:21]
	s_sub_u32 s22, s22, 1
	s_cmp_lg_u32 s22, 0
	s_cbranch_scc1 .Lgemm_T_loop
	s_waitcnt lgkmcnt(9)
	s_add_u32 m0, s11, 0x1e080
	v_mfma_f32_16x16x32_f16 v[82:85], v[134:137], v[86:89], v[82:85]
	global_load_lds_dwordx4 v[220:221], off offset:-128
	v_mfma_f32_16x16x32_f16 v[58:61], v[138:141], v[86:89], v[58:61]
	v_mfma_f32_16x16x32_f16 v[14:17], v[142:145], v[86:89], v[14:17]
	v_mfma_f32_16x16x32_f16 v[78:81], v[134:137], v[90:93], v[78:81]
	v_mfma_f32_16x16x32_f16 v[22:25], v[138:141], v[90:93], v[22:25]
	v_mfma_f32_16x16x32_f16 v[30:33], v[142:145], v[90:93], v[30:33]
	s_add_u32 m0, s11, 0x20080
	v_mfma_f32_16x16x32_f16 v[74:77], v[134:137], v[94:97], v[74:77]
	global_load_lds_dwordx4 v[224:225], off offset:-128
	v_mfma_f32_16x16x32_f16 v[18:21], v[138:141], v[94:97], v[18:21]
	v_mfma_f32_16x16x32_f16 v[26:29], v[142:145], v[94:97], v[26:29]
	v_mfma_f32_16x16x32_f16 v[70:73], v[134:137], v[98:101], v[70:73]
	v_mfma_f32_16x16x32_f16 v[46:49], v[138:141], v[98:101], v[46:49]
	v_mfma_f32_16x16x32_f16 v[240:243], v[142:145], v[98:101], v[240:243]
	s_add_u32 m0, s11, 0x22080
	v_mfma_f32_16x16x32_f16 v[66:69], v[134:137], v[102:105], v[66:69]
	global_load_lds_dwordx4 v[228:229], off offset:-128
	v_mfma_f32_16x16x32_f16 v[42:45], v[138:141], v[102:105], v[42:45]
	v_mfma_f32_16x16x32_f16 v[236:239], v[142:145], v[102:105], v[236:239]
	v_mfma_f32_16x16x32_f16 v[62:65], v[134:137], v[106:109], v[62:65]
	v_mfma_f32_16x16x32_f16 v[38:41], v[138:141], v[106:109], v[38:41]
	v_mfma_f32_16x16x32_f16 v[34:37], v[142:145], v[106:109], v[34:37]
	s_waitcnt vmcnt(6) lgkmcnt(0)
	s_barrier
	s_add_u32 m0, s11, 0x0
	ds_read_b128 v[134:137], v162 offset:49152
	global_load_lds_dwordx4 v[218:219], off
	v_mfma_f32_16x16x32_f16 v[82:85], v[146:149], v[110:113], v[82:85]
	ds_read_b128 v[138:141], v162 offset:51200
	v_mfma_f32_16x16x32_f16 v[58:61], v[150:153], v[110:113], v[58:61]
	ds_read_b128 v[142:145], v162 offset:53248
	v_mfma_f32_16x16x32_f16 v[14:17], v[154:157], v[110:113], v[14:17]
	ds_read_b128 v[86:89], v158 offset:49152
	v_mfma_f32_16x16x32_f16 v[78:81], v[146:149], v[114:117], v[78:81]
	ds_read_b128 v[90:93], v158 offset:51200
	v_mfma_f32_16x16x32_f16 v[22:25], v[150:153], v[114:117], v[22:25]
	ds_read_b128 v[94:97], v158 offset:53248
	v_mfma_f32_16x16x32_f16 v[30:33], v[154:157], v[114:117], v[30:33]
	s_add_u32 m0, s11, 0x2000
	ds_read_b128 v[98:101], v158 offset:55296
	global_load_lds_dwordx4 v[222:223], off
	v_mfma_f32_16x16x32_f16 v[74:77], v[146:149], v[118:121], v[74:77]
	ds_read_b128 v[102:105], v158 offset:57344
	v_mfma_f32_16x16x32_f16 v[18:21], v[150:153], v[118:121], v[18:21]
	ds_read_b128 v[106:109], v158 offset:59392
	v_mfma_f32_16x16x32_f16 v[26:29], v[154:157], v[118:121], v[26:29]
	ds_read_b128 v[110:113], v160 offset:49152
	v_mfma_f32_16x16x32_f16 v[70:73], v[146:149], v[122:125], v[70:73]
	ds_read_b128 v[114:117], v160 offset:51200
	v_mfma_f32_16x16x32_f16 v[46:49], v[150:153], v[122:125], v[46:49]
	v_mfma_f32_16x16x32_f16 v[240:243], v[154:157], v[122:125], v[240:243]
	s_add_u32 m0, s11, 0x4000
	ds_read_b128 v[118:121], v160 offset:53248
	global_load_lds_dwordx4 v[226:227], off
	v_mfma_f32_16x16x32_f16 v[66:69], v[146:149], v[126:129], v[66:69]
	ds_read_b128 v[122:125], v160 offset:55296
	v_mfma_f32_16x16x32_f16 v[42:45], v[150:153], v[126:129], v[42:45]
	v_mfma_f32_16x16x32_f16 v[236:239], v[154:157], v[126:129], v[236:239]
	ds_read_b128 v[126:129], v160 offset:57344
	v_mfma_f32_16x16x32_f16 v[62:65], v[146:149], v[130:133], v[62:65]
	v_mfma_f32_16x16x32_f16 v[38:41], v[150:153], v[130:133], v[38:41]
	v_mfma_f32_16x16x32_f16 v[34:37], v[154:157], v[130:133], v[34:37]
	ds_read_b128 v[130:133], v160 offset:59392
	ds_read_b128 v[146:149], v164 offset:49152
	ds_read_b128 v[150:153], v164 offset:51200
	ds_read_b128 v[154:157], v164 offset:53248
	s_waitcnt lgkmcnt(9)
	s_add_u32 m0, s11, 0x6000
	v_mfma_f32_16x16x32_f16 v[82:85], v[134:137], v[86:89], v[82:85]
	global_load_lds_dwordx4 v[220:221], off
	v_mfma_f32_16x16x32_f16 v[58:61], v[138:141], v[86:89], v[58:61]
	v_mfma_f32_16x16x32_f16 v[14:17], v[142:145], v[86:89], v[14:17]
	v_mfma_f32_16x16x32_f16 v[78:81], v[134:137], v[90:93], v[78:81]
	v_mfma_f32_16x16x32_f16 v[22:25], v[138:141], v[90:93], v[22:25]
	v_mfma_f32_16x16x32_f16 v[30:33], v[142:145], v[90:93], v[30:33]
	s_add_u32 m0, s11, 0x8000
	v_mfma_f32_16x16x32_f16 v[74:77], v[134:137], v[94:97], v[74:77]
	global_load_lds_dwordx4 v[224:225], off
	v_mfma_f32_16x16x32_f16 v[18:21], v[138:141], v[94:97], v[18:21]
	v_mfma_f32_16x16x32_f16 v[26:29], v[142:145], v[94:97], v[26:29]
	v_mfma_f32_16x16x32_f16 v[70:73], v[134:137], v[98:101], v[70:73]
	v_mfma_f32_16x16x32_f16 v[46:49], v[138:141], v[98:101], v[46:49]
	v_mfma_f32_16x16x32_f16 v[240:243], v[142:145], v[98:101], v[240:243]
	s_add_u32 m0, s11, 0xa000
	v_mfma_f32_16x16x32_f16 v[66:69], v[134:137], v[102:105], v[66:69]
	global_load_lds_dwordx4 v[228:229], off
	v_mfma_f32_16x16x32_f16 v[42:45], v[138:141], v[102:105], v[42:45]
	v_mfma_f32_16x16x32_f16 v[236:239], v[142:145], v[102:105], v[236:239]
	v_mfma_f32_16x16x32_f16 v[62:65], v[134:137], v[106:109], v[62:65]
	v_mfma_f32_16x16x32_f16 v[38:41], v[138:141], v[106:109], v[38:41]
	v_mfma_f32_16x16x32_f16 v[34:37], v[142:145], v[106:109], v[34:37]
	s_waitcnt vmcnt(6) lgkmcnt(0)
	s_barrier
	s_lshl_b32 s26, s17, 2
	s_add_u32 s26, s24, s26
	s_addc_u32 s27, s25, 0
	v_lshlrev_b32_e32 v50, 4, v231
	global_load_dwordx4 v[10:13], v50, s[26:27]
	global_load_dwordx4 v[6:9], v50, s[26:27] offset:64
	global_load_dwordx4 v[2:5], v50, s[26:27] offset:128
	ds_read_b128 v[134:137], v163
	v_mfma_f32_16x16x32_f16 v[82:85], v[146:149], v[110:113], v[82:85]
	ds_read_b128 v[138:141], v163 offset:2048
	v_mfma_f32_16x16x32_f16 v[58:61], v[150:153], v[110:113], v[58:61]
	ds_read_b128 v[142:145], v163 offset:4096
	v_mfma_f32_16x16x32_f16 v[14:17], v[154:157], v[110:113], v[14:17]
	ds_read_b128 v[86:89], v159
	v_mfma_f32_16x16x32_f16 v[78:81], v[146:149], v[114:117], v[78:81]
	ds_read_b128 v[90:93], v159 offset:2048
	v_mfma_f32_16x16x32_f16 v[22:25], v[150:153], v[114:117], v[22:25]
	ds_read_b128 v[94:97], v159 offset:4096
	v_mfma_f32_16x16x32_f16 v[30:33], v[154:157], v[114:117], v[30:33]
	ds_read_b128 v[98:101], v159 offset:6144
	v_mfma_f32_16x16x32_f16 v[74:77], v[146:149], v[118:121], v[74:77]
	ds_read_b128 v[102:105], v159 offset:8192
	v_mfma_f32_16x16x32_f16 v[18:21], v[150:153], v[118:121], v[18:21]
	ds_read_b128 v[106:109], v159 offset:10240
	v_mfma_f32_16x16x32_f16 v[26:29], v[154:157], v[118:121], v[26:29]
	ds_read_b128 v[110:113], v161
	v_mfma_f32_16x16x32_f16 v[70:73], v[146:149], v[122:125], v[70:73]
	ds_read_b128 v[114:117], v161 offset:2048
	v_mfma_f32_16x16x32_f16 v[46:49], v[150:153], v[122:125], v[46:49]
	v_mfma_f32_16x16x32_f16 v[240:243], v[154:157], v[122:125], v[240:243]
	ds_read_b128 v[118:121], v161 offset:4096
	v_mfma_f32_16x16x32_f16 v[66:69], v[146:149], v[126:129], v[66:69]
	ds_read_b128 v[122:125], v161 offset:6144
	v_mfma_f32_16x16x32_f16 v[42:45], v[150:153], v[126:129], v[42:45]
	v_mfma_f32_16x16x32_f16 v[236:239], v[154:157], v[126:129], v[236:239]
	ds_read_b128 v[126:129], v161 offset:8192
	v_mfma_f32_16x16x32_f16 v[62:65], v[146:149], v[130:133], v[62:65]
	v_mfma_f32_16x16x32_f16 v[38:41], v[150:153], v[130:133], v[38:41]
	v_mfma_f32_16x16x32_f16 v[34:37], v[154:157], v[130:133], v[34:37]
	ds_read_b128 v[130:133], v161 offset:10240
	ds_read_b128 v[146:149], v165
	ds_read_b128 v[150:153], v165 offset:2048
	ds_read_b128 v[154:157], v165 offset:4096
	s_waitcnt lgkmcnt(9)
	v_mfma_f32_16x16x32_f16 v[82:85], v[134:137], v[86:89], v[82:85]
	v_mfma_f32_16x16x32_f16 v[58:61], v[138:141], v[86:89], v[58:61]
	v_mfma_f32_16x16x32_f16 v[14:17], v[142:145], v[86:89], v[14:17]
	v_mfma_f32_16x16x32_f16 v[78:81], v[134:137], v[90:93], v[78:81]
	v_mfma_f32_16x16x32_f16 v[22:25], v[138:141], v[90:93], v[22:25]
	v_mfma_f32_16x16x32_f16 v[30:33], v[142:145], v[90:93], v[30:33]
	v_mfma_f32_16x16x32_f16 v[74:77], v[134:137], v[94:97], v[74:77]
	v_mfma_f32_16x16x32_f16 v[18:21], v[138:141], v[94:97], v[18:21]
	v_mfma_f32_16x16x32_f16 v[26:29], v[142:145], v[94:97], v[26:29]
	v_mfma_f32_16x16x32_f16 v[70:73], v[134:137], v[98:101], v[70:73]
	v_mfma_f32_16x16x32_f16 v[46:49], v[138:141], v[98:101], v[46:49]
	v_mfma_f32_16x16x32_f16 v[240:243], v[142:145], v[98:101], v[240:243]
	v_mfma_f32_16x16x32_f16 v[66:69], v[134:137], v[102:105], v[66:69]
	v_mfma_f32_16x16x32_f16 v[42:45], v[138:141], v[102:105], v[42:45]
	v_mfma_f32_16x16x32_f16 v[236:239], v[142:145], v[102:105], v[236:239]
	v_mfma_f32_16x16x32_f16 v[62:65], v[134:137], v[106:109], v[62:65]
	v_mfma_f32_16x16x32_f16 v[38:41], v[138:141], v[106:109], v[38:41]
	v_mfma_f32_16x16x32_f16 v[34:37], v[142:145], v[106:109], v[34:37]
	s_waitcnt vmcnt(3) lgkmcnt(0)
	s_barrier
	ds_read_b128 v[134:137], v162
	v_mfma_f32_16x16x32_f16 v[82:85], v[146:149], v[110:113], v[82:85]
	ds_read_b128 v[138:141], v162 offset:2048
	v_mfma_f32_16x16x32_f16 v[58:61], v[150:153], v[110:113], v[58:61]
	ds_read_b128 v[142:145], v162 offset:4096
	v_mfma_f32_16x16x32_f16 v[14:17], v[154:157], v[110:113], v[14:17]
	ds_read_b128 v[86:89], v158
	v_mfma_f32_16x16x32_f16 v[78:81], v[146:149], v[114:117], v[78:81]
	ds_read_b128 v[90:93], v158 offset:2048
	v_mfma_f32_16x16x32_f16 v[22:25], v[150:153], v[114:117], v[22:25]
	ds_read_b128 v[94:97], v158 offset:4096
	v_mfma_f32_16x16x32_f16 v[30:33], v[154:157], v[114:117], v[30:33]
	ds_read_b128 v[98:101], v158 offset:6144
	v_mfma_f32_16x16x32_f16 v[74:77], v[146:149], v[118:121], v[74:77]
	ds_read_b128 v[102:105], v158 offset:8192
	v_mfma_f32_16x16x32_f16 v[18:21], v[150:153], v[118:121], v[18:21]
	ds_read_b128 v[106:109], v158 offset:10240
	v_mfma_f32_16x16x32_f16 v[26:29], v[154:157], v[118:121], v[26:29]
	ds_read_b128 v[110:113], v160
	v_mfma_f32_16x16x32_f16 v[70:73], v[146:149], v[122:125], v[70:73]
	ds_read_b128 v[114:117], v160 offset:2048
	v_mfma_f32_16x16x32_f16 v[46:49], v[150:153], v[122:125], v[46:49]
	v_mfma_f32_16x16x32_f16 v[240:243], v[154:157], v[122:125], v[240:243]
	ds_read_b128 v[118:121], v160 offset:4096
	v_mfma_f32_16x16x32_f16 v[66:69], v[146:149], v[126:129], v[66:69]
	ds_read_b128 v[122:125], v160 offset:6144
	v_mfma_f32_16x16x32_f16 v[42:45], v[150:153], v[126:129], v[42:45]
	v_mfma_f32_16x16x32_f16 v[236:239], v[154:157], v[126:129], v[236:239]
	ds_read_b128 v[126:129], v160 offset:8192
	v_mfma_f32_16x16x32_f16 v[62:65], v[146:149], v[130:133], v[62:65]
	v_mfma_f32_16x16x32_f16 v[38:41], v[150:153], v[130:133], v[38:41]
	v_mfma_f32_16x16x32_f16 v[34:37], v[154:157], v[130:133], v[34:37]
	ds_read_b128 v[130:133], v160 offset:10240
	ds_read_b128 v[146:149], v164
	ds_read_b128 v[150:153], v164 offset:2048
	ds_read_b128 v[154:157], v164 offset:4096
	s_waitcnt lgkmcnt(9)
	v_mfma_f32_16x16x32_f16 v[82:85], v[134:137], v[86:89], v[82:85]
	v_mfma_f32_16x16x32_f16 v[58:61], v[138:141], v[86:89], v[58:61]
	v_mfma_f32_16x16x32_f16 v[14:17], v[142:145], v[86:89], v[14:17]
	v_mfma_f32_16x16x32_f16 v[78:81], v[134:137], v[90:93], v[78:81]
	v_mfma_f32_16x16x32_f16 v[22:25], v[138:141], v[90:93], v[22:25]
	v_mfma_f32_16x16x32_f16 v[30:33], v[142:145], v[90:93], v[30:33]
	v_mfma_f32_16x16x32_f16 v[74:77], v[134:137], v[94:97], v[74:77]
	v_mfma_f32_16x16x32_f16 v[18:21], v[138:141], v[94:97], v[18:21]
	v_mfma_f32_16x16x32_f16 v[26:29], v[142:145], v[94:97], v[26:29]
	v_mfma_f32_16x16x32_f16 v[70:73], v[134:137], v[98:101], v[70:73]
	v_mfma_f32_16x16x32_f16 v[46:49], v[138:141], v[98:101], v[46:49]
	v_mfma_f32_16x16x32_f16 v[240:243], v[142:145], v[98:101], v[240:243]
	v_mfma_f32_16x16x32_f16 v[66:69], v[134:137], v[102:105], v[66:69]
	v_mfma_f32_16x16x32_f16 v[42:45], v[138:141], v[102:105], v[42:45]
	v_mfma_f32_16x16x32_f16 v[236:239], v[142:145], v[102:105], v[236:239]
	v_mfma_f32_16x16x32_f16 v[62:65], v[134:137], v[106:109], v[62:65]
	v_mfma_f32_16x16x32_f16 v[38:41], v[138:141], v[106:109], v[38:41]
	v_mfma_f32_16x16x32_f16 v[34:37], v[142:145], v[106:109], v[34:37]
	s_waitcnt lgkmcnt(0)
	v_mfma_f32_16x16x32_f16 v[82:85], v[146:149], v[110:113], v[82:85]
	v_mfma_f32_16x16x32_f16 v[58:61], v[150:153], v[110:113], v[58:61]
	v_mfma_f32_16x16x32_f16 v[14:17], v[154:157], v[110:113], v[14:17]
	v_mfma_f32_16x16x32_f16 v[78:81], v[146:149], v[114:117], v[78:81]
	v_mfma_f32_16x16x32_f16 v[22:25], v[150:153], v[114:117], v[22:25]
	v_mfma_f32_16x16x32_f16 v[30:33], v[154:157], v[114:117], v[30:33]
	v_mfma_f32_16x16x32_f16 v[74:77], v[146:149], v[118:121], v[74:77]
	v_mfma_f32_16x16x32_f16 v[18:21], v[150:153], v[118:121], v[18:21]
	v_mfma_f32_16x16x32_f16 v[26:29], v[154:157], v[118:121], v[26:29]
	v_mfma_f32_16x16x32_f16 v[70:73], v[146:149], v[122:125], v[70:73]
	v_mfma_f32_16x16x32_f16 v[46:49], v[150:153], v[122:125], v[46:49]
	v_mfma_f32_16x16x32_f16 v[240:243], v[154:157], v[122:125], v[240:243]
	v_mfma_f32_16x16x32_f16 v[66:69], v[146:149], v[126:129], v[66:69]
	v_mfma_f32_16x16x32_f16 v[42:45], v[150:153], v[126:129], v[42:45]
	v_mfma_f32_16x16x32_f16 v[236:239], v[154:157], v[126:129], v[236:239]
	v_mfma_f32_16x16x32_f16 v[62:65], v[146:149], v[130:133], v[62:65]
	v_mfma_f32_16x16x32_f16 v[38:41], v[150:153], v[130:133], v[38:41]
	v_mfma_f32_16x16x32_f16 v[34:37], v[154:157], v[130:133], v[34:37]
	s_branch .LBB1_76
.Lgemm_N_loop:
	s_waitcnt lgkmcnt(9)
	s_add_u32 m0, s11, 0x1e080
	v_mfma_f32_16x16x32_f16 v[82:85], v[86:89], v[134:137], v[82:85]
	global_load_lds_dwordx4 v[220:221], off offset:-128
	v_mfma_f32_16x16x32_f16 v[58:61], v[86:89], v[138:141], v[58:61]
	v_mfma_f32_16x16x32_f16 v[14:17], v[86:89], v[142:145], v[14:17]
	v_mfma_f32_16x16x32_f16 v[78:81], v[90:93], v[134:137], v[78:81]
	v_mfma_f32_16x16x32_f16 v[22:25], v[90:93], v[138:141], v[22:25]
	v_mfma_f32_16x16x32_f16 v[30:33], v[90:93], v[142:145], v[30:33]
	s_add_u32 m0, s11, 0x20080
	v_mfma_f32_16x16x32_f16 v[74:77], v[94:97], v[134:137], v[74:77]
	global_load_lds_dwordx4 v[224:225], off offset:-128
	v_mfma_f32_16x16x32_f16 v[18:21], v[94:97], v[138:141], v[18:21]
	v_mfma_f32_16x16x32_f16 v[26:29], v[94:97], v[142:145], v[26:29]
	v_mfma_f32_16x16x32_f16 v[70:73], v[98:101], v[134:137], v[70:73]
	v_mfma_f32_16x16x32_f16 v[46:49], v[98:101], v[138:141], v[46:49]
	v_mfma_f32_16x16x32_f16 v[240:243], v[98:101], v[142:145], v[240:243]
	s_add_u32 m0, s11, 0x22080
	v_mfma_f32_16x16x32_f16 v[66:69], v[102:105], v[134:137], v[66:69]
	global_load_lds_dwordx4 v[228:229], off offset:-128
	v_mfma_f32_16x16x32_f16 v[42:45], v[102:105], v[138:141], v[42:45]
	v_mfma_f32_16x16x32_f16 v[236:239], v[102:105], v[142:145], v[236:239]
	v_mfma_f32_16x16x32_f16 v[62:65], v[106:109], v[134:137], v[62:65]
	v_mfma_f32_16x16x32_f16 v[38:41], v[106:109], v[138:141], v[38:41]
	v_mfma_f32_16x16x32_f16 v[34:37], v[106:109], v[142:145], v[34:37]
	s_waitcnt vmcnt(6) lgkmcnt(0)
	s_barrier
	s_add_u32 m0, s11, 0x0
	ds_read_b128 v[134:137], v162 offset:49152
	global_load_lds_dwordx4 v[218:219], off
	v_mfma_f32_16x16x32_f16 v[82:85], v[110:113], v[146:149], v[82:85]
	ds_read_b128 v[138:141], v162 offset:51200
	v_mfma_f32_16x16x32_f16 v[58:61], v[110:113], v[150:153], v[58:61]
	ds_read_b128 v[142:145], v162 offset:53248
	v_mfma_f32_16x16x32_f16 v[14:17], v[110:113], v[154:157], v[14:17]
	ds_read_b128 v[86:89], v158 offset:49152
	v_mfma_f32_16x16x32_f16 v[78:81], v[114:117], v[146:149], v[78:81]
	ds_read_b128 v[90:93], v158 offset:51200
	v_mfma_f32_16x16x32_f16 v[22:25], v[114:117], v[150:153], v[22:25]
	ds_read_b128 v[94:97], v158 offset:53248
	v_mfma_f32_16x16x32_f16 v[30:33], v[114:117], v[154:157], v[30:33]
	s_add_u32 m0, s11, 0x2000
	ds_read_b128 v[98:101], v158 offset:55296
	global_load_lds_dwordx4 v[222:223], off
	v_mfma_f32_16x16x32_f16 v[74:77], v[118:121], v[146:149], v[74:77]
	ds_read_b128 v[102:105], v158 offset:57344
	v_mfma_f32_16x16x32_f16 v[18:21], v[118:121], v[150:153], v[18:21]
	ds_read_b128 v[106:109], v158 offset:59392
	v_mfma_f32_16x16x32_f16 v[26:29], v[118:121], v[154:157], v[26:29]
	ds_read_b128 v[110:113], v160 offset:49152
	v_mfma_f32_16x16x32_f16 v[70:73], v[122:125], v[146:149], v[70:73]
	ds_read_b128 v[114:117], v160 offset:51200
	v_mfma_f32_16x16x32_f16 v[46:49], v[122:125], v[150:153], v[46:49]
	v_mfma_f32_16x16x32_f16 v[240:243], v[122:125], v[154:157], v[240:243]
	s_add_u32 m0, s11, 0x4000
	ds_read_b128 v[118:121], v160 offset:53248
	global_load_lds_dwordx4 v[226:227], off
	v_mfma_f32_16x16x32_f16 v[66:69], v[126:129], v[146:149], v[66:69]
	ds_read_b128 v[122:125], v160 offset:55296
	v_mfma_f32_16x16x32_f16 v[42:45], v[126:129], v[150:153], v[42:45]
	v_mfma_f32_16x16x32_f16 v[236:239], v[126:129], v[154:157], v[236:239]
	ds_read_b128 v[126:129], v160 offset:57344
	v_mfma_f32_16x16x32_f16 v[62:65], v[130:133], v[146:149], v[62:65]
	v_mfma_f32_16x16x32_f16 v[38:41], v[130:133], v[150:153], v[38:41]
	v_mfma_f32_16x16x32_f16 v[34:37], v[130:133], v[154:157], v[34:37]
	ds_read_b128 v[130:133], v160 offset:59392
	ds_read_b128 v[146:149], v164 offset:49152
	ds_read_b128 v[150:153], v164 offset:51200
	ds_read_b128 v[154:157], v164 offset:53248
	s_waitcnt lgkmcnt(9)
	s_add_u32 m0, s11, 0x6000
	v_mfma_f32_16x16x32_f16 v[82:85], v[86:89], v[134:137], v[82:85]
	global_load_lds_dwordx4 v[220:221], off
	v_mfma_f32_16x16x32_f16 v[58:61], v[86:89], v[138:141], v[58:61]
	v_mfma_f32_16x16x32_f16 v[14:17], v[86:89], v[142:145], v[14:17]
	v_mfma_f32_16x16x32_f16 v[78:81], v[90:93], v[134:137], v[78:81]
	v_mfma_f32_16x16x32_f16 v[22:25], v[90:93], v[138:141], v[22:25]
	v_mfma_f32_16x16x32_f16 v[30:33], v[90:93], v[142:145], v[30:33]
	s_add_u32 m0, s11, 0x8000
	v_mfma_f32_16x16x32_f16 v[74:77], v[94:97], v[134:137], v[74:77]
	global_load_lds_dwordx4 v[224:225], off
	v_mfma_f32_16x16x32_f16 v[18:21], v[94:97], v[138:141], v[18:21]
	v_mfma_f32_16x16x32_f16 v[26:29], v[94:97], v[142:145], v[26:29]
	v_mfma_f32_16x16x32_f16 v[70:73], v[98:101], v[134:137], v[70:73]
	v_mfma_f32_16x16x32_f16 v[46:49], v[98:101], v[138:141], v[46:49]
	v_mfma_f32_16x16x32_f16 v[240:243], v[98:101], v[142:145], v[240:243]
	s_add_u32 m0, s11, 0xa000
	v_mfma_f32_16x16x32_f16 v[66:69], v[102:105], v[134:137], v[66:69]
	global_load_lds_dwordx4 v[228:229], off
	v_mfma_f32_16x16x32_f16 v[42:45], v[102:105], v[138:141], v[42:45]
	v_mfma_f32_16x16x32_f16 v[236:239], v[102:105], v[142:145], v[236:239]
	v_mfma_f32_16x16x32_f16 v[62:65], v[106:109], v[134:137], v[62:65]
	v_mfma_f32_16x16x32_f16 v[38:41], v[106:109], v[138:141], v[38:41]
	v_mfma_f32_16x16x32_f16 v[34:37], v[106:109], v[142:145], v[34:37]
	s_waitcnt vmcnt(6) lgkmcnt(0)
	s_barrier
	s_add_u32 m0, s11, 0xbf80
	ds_read_b128 v[134:137], v163
	global_load_lds_dwordx4 v[218:219], off offset:128
	v_mfma_f32_16x16x32_f16 v[82:85], v[110:113], v[146:149], v[82:85]
	ds_read_b128 v[138:141], v163 offset:2048
	v_mfma_f32_16x16x32_f16 v[58:61], v[110:113], v[150:153], v[58:61]
	ds_read_b128 v[142:145], v163 offset:4096
	v_mfma_f32_16x16x32_f16 v[14:17], v[110:113], v[154:157], v[14:17]
	ds_read_b128 v[86:89], v159
	v_mfma_f32_16x16x32_f16 v[78:81], v[114:117], v[146:149], v[78:81]
	ds_read_b128 v[90:93], v159 offset:2048
	v_mfma_f32_16x16x32_f16 v[22:25], v[114:117], v[150:153], v[22:25]
	ds_read_b128 v[94:97], v159 offset:4096
	v_mfma_f32_16x16x32_f16 v[30:33], v[114:117], v[154:157], v[30:33]
	s_add_u32 m0, s11, 0xdf80
	ds_read_b128 v[98:101], v159 offset:6144
	global_load_lds_dwordx4 v[222:223], off offset:128
	v_mfma_f32_16x16x32_f16 v[74:77], v[118:121], v[146:149], v[74:77]
	ds_read_b128 v[102:105], v159 offset:8192
	v_mfma_f32_16x16x32_f16 v[18:21], v[118:121], v[150:153], v[18:21]
	ds_read_b128 v[106:109], v159 offset:10240
	v_mfma_f32_16x16x32_f16 v[26:29], v[118:121], v[154:157], v[26:29]
	ds_read_b128 v[110:113], v161
	v_mfma_f32_16x16x32_f16 v[70:73], v[122:125], v[146:149], v[70:73]
	ds_read_b128 v[114:117], v161 offset:2048
	v_mfma_f32_16x16x32_f16 v[46:49], v[122:125], v[150:153], v[46:49]
	v_mfma_f32_16x16x32_f16 v[240:243], v[122:125], v[154:157], v[240:243]
	s_add_u32 m0, s11, 0xff80
	ds_read_b128 v[118:121], v161 offset:4096
	global_load_lds_dwordx4 v[226:227], off offset:128
	v_mfma_f32_16x16x32_f16 v[66:69], v[126:129], v[146:149], v[66:69]
	ds_read_b128 v[122:125], v161 offset:6144
	v_mfma_f32_16x16x32_f16 v[42:45], v[126:129], v[150:153], v[42:45]
	v_mfma_f32_16x16x32_f16 v[236:239], v[126:129], v[154:157], v[236:239]
	ds_read_b128 v[126:129], v161 offset:8192
	v_mfma_f32_16x16x32_f16 v[62:65], v[130:133], v[146:149], v[62:65]
	v_mfma_f32_16x16x32_f16 v[38:41], v[130:133], v[150:153], v[38:41]
	v_mfma_f32_16x16x32_f16 v[34:37], v[130:133], v[154:157], v[34:37]
	ds_read_b128 v[130:133], v161 offset:10240
	ds_read_b128 v[146:149], v165
	ds_read_b128 v[150:153], v165 offset:2048
	ds_read_b128 v[154:157], v165 offset:4096
	s_waitcnt lgkmcnt(9)
	s_add_u32 m0, s11, 0x11f80
	v_mfma_f32_16x16x32_f16 v[82:85], v[86:89], v[134:137], v[82:85]
	global_load_lds_dwordx4 v[220:221], off offset:128
	v_mfma_f32_16x16x32_f16 v[58:61], v[86:89], v[138:141], v[58:61]
	v_mfma_f32_16x16x32_f16 v[14:17], v[86:89], v[142:145], v[14:17]
	v_mfma_f32_16x16x32_f16 v[78:81], v[90:93], v[134:137], v[78:81]
	v_mfma_f32_16x16x32_f16 v[22:25], v[90:93], v[138:141], v[22:25]
	v_mfma_f32_16x16x32_f16 v[30:33], v[90:93], v[142:145], v[30:33]
	s_add_u32 m0, s11, 0x13f80
	v_mfma_f32_16x16x32_f16 v[74:77], v[94:97], v[134:137], v[74:77]
	global_load_lds_dwordx4 v[224:225], off offset:128
	v_mfma_f32_16x16x32_f16 v[18:21], v[94:97], v[138:141], v[18:21]
	v_mfma_f32_16x16x32_f16 v[26:29], v[94:97], v[142:145], v[26:29]
	v_mfma_f32_16x16x32_f16 v[70:73], v[98:101], v[134:137], v[70:73]
	v_mfma_f32_16x16x32_f16 v[46:49], v[98:101], v[138:141], v[46:49]
	v_mfma_f32_16x16x32_f16 v[240:243], v[98:101], v[142:145], v[240:243]
	s_add_u32 m0, s11, 0x15f80
	v_mfma_f32_16x16x32_f16 v[66:69], v[102:105], v[134:137], v[66:69]
	global_load_lds_dwordx4 v[228:229], off offset:128
	v_mfma_f32_16x16x32_f16 v[42:45], v[102:105], v[138:141], v[42:45]
	v_mfma_f32_16x16x32_f16 v[236:239], v[102:105], v[142:145], v[236:239]
	v_mfma_f32_16x16x32_f16 v[62:65], v[106:109], v[134:137], v[62:65]
	v_mfma_f32_16x16x32_f16 v[38:41], v[106:109], v[138:141], v[38:41]
	v_mfma_f32_16x16x32_f16 v[34:37], v[106:109], v[142:145], v[34:37]
	s_waitcnt vmcnt(6) lgkmcnt(0)
	s_barrier
	s_add_u32 m0, s11, 0x17f00
	ds_read_b128 v[134:137], v162
	global_load_lds_dwordx4 v[218:219], off offset:256
	v_mfma_f32_16x16x32_f16 v[82:85], v[110:113], v[146:149], v[82:85]
	ds_read_b128 v[138:141], v162 offset:2048
	v_mfma_f32_16x16x32_f16 v[58:61], v[110:113], v[150:153], v[58:61]
	ds_read_b128 v[142:145], v162 offset:4096
	v_mfma_f32_16x16x32_f16 v[14:17], v[110:113], v[154:157], v[14:17]
	ds_read_b128 v[86:89], v158
	v_mfma_f32_16x16x32_f16 v[78:81], v[114:117], v[146:149], v[78:81]
	ds_read_b128 v[90:93], v158 offset:2048
	v_mfma_f32_16x16x32_f16 v[22:25], v[114:117], v[150:153], v[22:25]
	ds_read_b128 v[94:97], v158 offset:4096
	v_mfma_f32_16x16x32_f16 v[30:33], v[114:117], v[154:157], v[30:33]
	s_add_u32 m0, s11, 0x19f00
	ds_read_b128 v[98:101], v158 offset:6144
	global_load_lds_dwordx4 v[222:223], off offset:256
	v_mfma_f32_16x16x32_f16 v[74:77], v[118:121], v[146:149], v[74:77]
	ds_read_b128 v[102:105], v158 offset:8192
	v_mfma_f32_16x16x32_f16 v[18:21], v[118:121], v[150:153], v[18:21]
	ds_read_b128 v[106:109], v158 offset:10240
	v_mfma_f32_16x16x32_f16 v[26:29], v[118:121], v[154:157], v[26:29]
	ds_read_b128 v[110:113], v160
	v_mfma_f32_16x16x32_f16 v[70:73], v[122:125], v[146:149], v[70:73]
	ds_read_b128 v[114:117], v160 offset:2048
	v_mfma_f32_16x16x32_f16 v[46:49], v[122:125], v[150:153], v[46:49]
	v_mfma_f32_16x16x32_f16 v[240:243], v[122:125], v[154:157], v[240:243]
	s_add_u32 m0, s11, 0x1bf00
	ds_read_b128 v[118:121], v160 offset:4096
	global_load_lds_dwordx4 v[226:227], off offset:256
	v_mfma_f32_16x16x32_f16 v[66:69], v[126:129], v[146:149], v[66:69]
	ds_read_b128 v[122:125], v160 offset:6144
	v_mfma_f32_16x16x32_f16 v[42:45], v[126:129], v[150:153], v[42:45]
	v_mfma_f32_16x16x32_f16 v[236:239], v[126:129], v[154:157], v[236:239]
	ds_read_b128 v[126:129], v160 offset:8192
	v_mfma_f32_16x16x32_f16 v[62:65], v[130:133], v[146:149], v[62:65]
	v_mfma_f32_16x16x32_f16 v[38:41], v[130:133], v[150:153], v[38:41]
	v_mfma_f32_16x16x32_f16 v[34:37], v[130:133], v[154:157], v[34:37]
	ds_read_b128 v[130:133], v160 offset:10240
	ds_read_b128 v[146:149], v164
	ds_read_b128 v[150:153], v164 offset:2048
	ds_read_b128 v[154:157], v164 offset:4096
	v_lshl_add_u64 v[218:219], v[218:219], 0, s[20:21]
	v_lshl_add_u64 v[222:223], v[222:223], 0, s[20:21]
	v_lshl_add_u64 v[226:227], v[226:227], 0, s[20:21]
	v_lshl_add_u64 v[220:221], v[220:221], 0, s[20:21]
	v_lshl_add_u64 v[224:225], v[224:225], 0, s[20:21]
	v_lshl_add_u64 v[228:229], v[228:229], 0, s[20:21]
	s_sub_u32 s22, s22, 1
	s_cmp_lg_u32 s22, 0
	s_cbranch_scc1 .Lgemm_N_loop
	s_waitcnt lgkmcnt(9)
	s_add_u32 m0, s11, 0x1e080
	v_mfma_f32_16x16x32_f16 v[82:85], v[86:89], v[134:137], v[82:85]
	global_load_lds_dwordx4 v[220:221], off offset:-128
	v_mfma_f32_16x16x32_f16 v[58:61], v[86:89], v[138:141], v[58:61]
	v_mfma_f32_16x16x32_f16 v[14:17], v[86:89], v[142:145], v[14:17]
	v_mfma_f32_16x16x32_f16 v[78:81], v[90:93], v[134:137], v[78:81]
	v_mfma_f32_16x16x32_f16 v[22:25], v[90:93], v[138:141], v[22:25]
	v_mfma_f32_16x16x32_f16 v[30:33], v[90:93], v[142:145], v[30:33]
	s_add_u32 m0, s11, 0x20080
	v_mfma_f32_16x16x32_f16 v[74:77], v[94:97], v[134:137], v[74:77]
	global_load_lds_dwordx4 v[224:225], off offset:-128
	v_mfma_f32_16x16x32_f16 v[18:21], v[94:97], v[138:141], v[18:21]
	v_mfma_f32_16x16x32_f16 v[26:29], v[94:97], v[142:145], v[26:29]
	v_mfma_f32_16x16x32_f16 v[70:73], v[98:101], v[134:137], v[70:73]
	v_mfma_f32_16x16x32_f16 v[46:49], v[98:101], v[138:141], v[46:49]
	v_mfma_f32_16x16x32_f16 v[240:243], v[98:101], v[142:145], v[240:243]
	s_add_u32 m0, s11, 0x22080
	v_mfma_f32_16x16x32_f16 v[66:69], v[102:105], v[134:137], v[66:69]
	global_load_lds_dwordx4 v[228:229], off offset:-128
	v_mfma_f32_16x16x32_f16 v[42:45], v[102:105], v[138:141], v[42:45]
	v_mfma_f32_16x16x32_f16 v[236:239], v[102:105], v[142:145], v[236:239]
	v_mfma_f32_16x16x32_f16 v[62:65], v[106:109], v[134:137], v[62:65]
	v_mfma_f32_16x16x32_f16 v[38:41], v[106:109], v[138:141], v[38:41]
	v_mfma_f32_16x16x32_f16 v[34:37], v[106:109], v[142:145], v[34:37]
	s_waitcnt vmcnt(6) lgkmcnt(0)
	s_barrier
	s_add_u32 m0, s11, 0x0
	ds_read_b128 v[134:137], v162 offset:49152
	global_load_lds_dwordx4 v[218:219], off
	v_mfma_f32_16x16x32_f16 v[82:85], v[110:113], v[146:149], v[82:85]
	ds_read_b128 v[138:141], v162 offset:51200
	v_mfma_f32_16x16x32_f16 v[58:61], v[110:113], v[150:153], v[58:61]
	ds_read_b128 v[142:145], v162 offset:53248
	v_mfma_f32_16x16x32_f16 v[14:17], v[110:113], v[154:157], v[14:17]
	ds_read_b128 v[86:89], v158 offset:49152
	v_mfma_f32_16x16x32_f16 v[78:81], v[114:117], v[146:149], v[78:81]
	ds_read_b128 v[90:93], v158 offset:51200
	v_mfma_f32_16x16x32_f16 v[22:25], v[114:117], v[150:153], v[22:25]
	ds_read_b128 v[94:97], v158 offset:53248
	v_mfma_f32_16x16x32_f16 v[30:33], v[114:117], v[154:157], v[30:33]
	s_add_u32 m0, s11, 0x2000
	ds_read_b128 v[98:101], v158 offset:55296
	global_load_lds_dwordx4 v[222:223], off
	v_mfma_f32_16x16x32_f16 v[74:77], v[118:121], v[146:149], v[74:77]
	ds_read_b128 v[102:105], v158 offset:57344
	v_mfma_f32_16x16x32_f16 v[18:21], v[118:121], v[150:153], v[18:21]
	ds_read_b128 v[106:109], v158 offset:59392
	v_mfma_f32_16x16x32_f16 v[26:29], v[118:121], v[154:157], v[26:29]
	ds_read_b128 v[110:113], v160 offset:49152
	v_mfma_f32_16x16x32_f16 v[70:73], v[122:125], v[146:149], v[70:73]
	ds_read_b128 v[114:117], v160 offset:51200
	v_mfma_f32_16x16x32_f16 v[46:49], v[122:125], v[150:153], v[46:49]
	v_mfma_f32_16x16x32_f16 v[240:243], v[122:125], v[154:157], v[240:243]
	s_add_u32 m0, s11, 0x4000
	ds_read_b128 v[118:121], v160 offset:53248
	global_load_lds_dwordx4 v[226:227], off
	v_mfma_f32_16x16x32_f16 v[66:69], v[126:129], v[146:149], v[66:69]
	ds_read_b128 v[122:125], v160 offset:55296
	v_mfma_f32_16x16x32_f16 v[42:45], v[126:129], v[150:153], v[42:45]
	v_mfma_f32_16x16x32_f16 v[236:239], v[126:129], v[154:157], v[236:239]
	ds_read_b128 v[126:129], v160 offset:57344
	v_mfma_f32_16x16x32_f16 v[62:65], v[130:133], v[146:149], v[62:65]
	v_mfma_f32_16x16x32_f16 v[38:41], v[130:133], v[150:153], v[38:41]
	v_mfma_f32_16x16x32_f16 v[34:37], v[130:133], v[154:157], v[34:37]
	ds_read_b128 v[130:133], v160 offset:59392
	ds_read_b128 v[146:149], v164 offset:49152
	ds_read_b128 v[150:153], v164 offset:51200
	ds_read_b128 v[154:157], v164 offset:53248
	s_waitcnt lgkmcnt(9)
	s_add_u32 m0, s11, 0x6000
	v_mfma_f32_16x16x32_f16 v[82:85], v[86:89], v[134:137], v[82:85]
	global_load_lds_dwordx4 v[220:221], off
	v_mfma_f32_16x16x32_f16 v[58:61], v[86:89], v[138:141], v[58:61]
	v_mfma_f32_16x16x32_f16 v[14:17], v[86:89], v[142:145], v[14:17]
	v_mfma_f32_16x16x32_f16 v[78:81], v[90:93], v[134:137], v[78:81]
	v_mfma_f32_16x16x32_f16 v[22:25], v[90:93], v[138:141], v[22:25]
	v_mfma_f32_16x16x32_f16 v[30:33], v[90:93], v[142:145], v[30:33]
	s_add_u32 m0, s11, 0x8000
	v_mfma_f32_16x16x32_f16 v[74:77], v[94:97], v[134:137], v[74:77]
	global_load_lds_dwordx4 v[224:225], off
	v_mfma_f32_16x16x32_f16 v[18:21], v[94:97], v[138:141], v[18:21]
	v_mfma_f32_16x16x32_f16 v[26:29], v[94:97], v[142:145], v[26:29]
	v_mfma_f32_16x16x32_f16 v[70:73], v[98:101], v[134:137], v[70:73]
	v_mfma_f32_16x16x32_f16 v[46:49], v[98:101], v[138:141], v[46:49]
	v_mfma_f32_16x16x32_f16 v[240:243], v[98:101], v[142:145], v[240:243]
	s_add_u32 m0, s11, 0xa000
	v_mfma_f32_16x16x32_f16 v[66:69], v[102:105], v[134:137], v[66:69]
	global_load_lds_dwordx4 v[228:229], off
	v_mfma_f32_16x16x32_f16 v[42:45], v[102:105], v[138:141], v[42:45]
	v_mfma_f32_16x16x32_f16 v[236:239], v[102:105], v[142:145], v[236:239]
	v_mfma_f32_16x16x32_f16 v[62:65], v[106:109], v[134:137], v[62:65]
	v_mfma_f32_16x16x32_f16 v[38:41], v[106:109], v[138:141], v[38:41]
	v_mfma_f32_16x16x32_f16 v[34:37], v[106:109], v[142:145], v[34:37]
	s_waitcnt vmcnt(6) lgkmcnt(0)
	s_barrier
	s_lshl_b32 s26, s17, 2
	s_add_u32 s26, s24, s26
	s_addc_u32 s27, s25, 0
	v_lshlrev_b32_e32 v50, 2, v1
	global_load_dword v234, v50, s[26:27]
	global_load_dword v232, v50, s[26:27] offset:64
	global_load_dword v230, v50, s[26:27] offset:128
	ds_read_b128 v[134:137], v163
	v_mfma_f32_16x16x32_f16 v[82:85], v[110:113], v[146:149], v[82:85]
	ds_read_b128 v[138:141], v163 offset:2048
	v_mfma_f32_16x16x32_f16 v[58:61], v[110:113], v[150:153], v[58:61]
	ds_read_b128 v[142:145], v163 offset:4096
	v_mfma_f32_16x16x32_f16 v[14:17], v[110:113], v[154:157], v[14:17]
	ds_read_b128 v[86:89], v159
	v_mfma_f32_16x16x32_f16 v[78:81], v[114:117], v[146:149], v[78:81]
	ds_read_b128 v[90:93], v159 offset:2048
	v_mfma_f32_16x16x32_f16 v[22:25], v[114:117], v[150:153], v[22:25]
	ds_read_b128 v[94:97], v159 offset:4096
	v_mfma_f32_16x16x32_f16 v[30:33], v[114:117], v[154:157], v[30:33]
	ds_read_b128 v[98:101], v159 offset:6144
	v_mfma_f32_16x16x32_f16 v[74:77], v[118:121], v[146:149], v[74:77]
	ds_read_b128 v[102:105], v159 offset:8192
	v_mfma_f32_16x16x32_f16 v[18:21], v[118:121], v[150:153], v[18:21]
	ds_read_b128 v[106:109], v159 offset:10240
	v_mfma_f32_16x16x32_f16 v[26:29], v[118:121], v[154:157], v[26:29]
	ds_read_b128 v[110:113], v161
	v_mfma_f32_16x16x32_f16 v[70:73], v[122:125], v[146:149], v[70:73]
	ds_read_b128 v[114:117], v161 offset:2048
	v_mfma_f32_16x16x32_f16 v[46:49], v[122:125], v[150:153], v[46:49]
	v_mfma_f32_16x16x32_f16 v[240:243], v[122:125], v[154:157], v[240:243]
	ds_read_b128 v[118:121], v161 offset:4096
	v_mfma_f32_16x16x32_f16 v[66:69], v[126:129], v[146:149], v[66:69]
	ds_read_b128 v[122:125], v161 offset:6144
	v_mfma_f32_16x16x32_f16 v[42:45], v[126:129], v[150:153], v[42:45]
	v_mfma_f32_16x16x32_f16 v[236:239], v[126:129], v[154:157], v[236:239]
	ds_read_b128 v[126:129], v161 offset:8192
	v_mfma_f32_16x16x32_f16 v[62:65], v[130:133], v[146:149], v[62:65]
	v_mfma_f32_16x16x32_f16 v[38:41], v[130:133], v[150:153], v[38:41]
	v_mfma_f32_16x16x32_f16 v[34:37], v[130:133], v[154:157], v[34:37]
	ds_read_b128 v[130:133], v161 offset:10240
	ds_read_b128 v[146:149], v165
	ds_read_b128 v[150:153], v165 offset:2048
	ds_read_b128 v[154:157], v165 offset:4096
	s_waitcnt lgkmcnt(9)
	v_mfma_f32_16x16x32_f16 v[82:85], v[86:89], v[134:137], v[82:85]
	v_mfma_f32_16x16x32_f16 v[58:61], v[86:89], v[138:141], v[58:61]
	v_mfma_f32_16x16x32_f16 v[14:17], v[86:89], v[142:145], v[14:17]
	v_mfma_f32_16x16x32_f16 v[78:81], v[90:93], v[134:137], v[78:81]
	v_mfma_f32_16x16x32_f16 v[22:25], v[90:93], v[138:141], v[22:25]
	v_mfma_f32_16x16x32_f16 v[30:33], v[90:93], v[142:145], v[30:33]
	v_mfma_f32_16x16x32_f16 v[74:77], v[94:97], v[134:137], v[74:77]
	v_mfma_f32_16x16x32_f16 v[18:21], v[94:97], v[138:141], v[18:21]
	v_mfma_f32_16x16x32_f16 v[26:29], v[94:97], v[142:145], v[26:29]
	v_mfma_f32_16x16x32_f16 v[70:73], v[98:101], v[134:137], v[70:73]
	v_mfma_f32_16x16x32_f16 v[46:49], v[98:101], v[138:141], v[46:49]
	v_mfma_f32_16x16x32_f16 v[240:243], v[98:101], v[142:145], v[240:243]
	v_mfma_f32_16x16x32_f16 v[66:69], v[102:105], v[134:137], v[66:69]
	v_mfma_f32_16x16x32_f16 v[42:45], v[102:105], v[138:141], v[42:45]
	v_mfma_f32_16x16x32_f16 v[236:239], v[102:105], v[142:145], v[236:239]
	v_mfma_f32_16x16x32_f16 v[62:65], v[106:109], v[134:137], v[62:65]
	v_mfma_f32_16x16x32_f16 v[38:41], v[106:109], v[138:141], v[38:41]
	v_mfma_f32_16x16x32_f16 v[34:37], v[106:109], v[142:145], v[34:37]
	s_waitcnt vmcnt(3) lgkmcnt(0)
	s_barrier
	ds_read_b128 v[134:137], v162
	v_mfma_f32_16x16x32_f16 v[82:85], v[110:113], v[146:149], v[82:85]
	ds_read_b128 v[138:141], v162 offset:2048
	v_mfma_f32_16x16x32_f16 v[58:61], v[110:113], v[150:153], v[58:61]
	ds_read_b128 v[142:145], v162 offset:4096
	v_mfma_f32_16x16x32_f16 v[14:17], v[110:113], v[154:157], v[14:17]
	ds_read_b128 v[86:89], v158
	v_mfma_f32_16x16x32_f16 v[78:81], v[114:117], v[146:149], v[78:81]
	ds_read_b128 v[90:93], v158 offset:2048
	v_mfma_f32_16x16x32_f16 v[22:25], v[114:117], v[150:153], v[22:25]
	ds_read_b128 v[94:97], v158 offset:4096
	v_mfma_f32_16x16x32_f16 v[30:33], v[114:117], v[154:157], v[30:33]
	ds_read_b128 v[98:101], v158 offset:6144
	v_mfma_f32_16x16x32_f16 v[74:77], v[118:121], v[146:149], v[74:77]
	ds_read_b128 v[102:105], v158 offset:8192
	v_mfma_f32_16x16x32_f16 v[18:21], v[118:121], v[150:153], v[18:21]
	ds_read_b128 v[106:109], v158 offset:10240
	v_mfma_f32_16x16x32_f16 v[26:29], v[118:121], v[154:157], v[26:29]
	ds_read_b128 v[110:113], v160
	v_mfma_f32_16x16x32_f16 v[70:73], v[122:125], v[146:149], v[70:73]
	ds_read_b128 v[114:117], v160 offset:2048
	v_mfma_f32_16x16x32_f16 v[46:49], v[122:125], v[150:153], v[46:49]
	v_mfma_f32_16x16x32_f16 v[240:243], v[122:125], v[154:157], v[240:243]
	ds_read_b128 v[118:121], v160 offset:4096
	v_mfma_f32_16x16x32_f16 v[66:69], v[126:129], v[146:149], v[66:69]
	ds_read_b128 v[122:125], v160 offset:6144
	v_mfma_f32_16x16x32_f16 v[42:45], v[126:129], v[150:153], v[42:45]
	v_mfma_f32_16x16x32_f16 v[236:239], v[126:129], v[154:157], v[236:239]
	ds_read_b128 v[126:129], v160 offset:8192
	v_mfma_f32_16x16x32_f16 v[62:65], v[130:133], v[146:149], v[62:65]
	v_mfma_f32_16x16x32_f16 v[38:41], v[130:133], v[150:153], v[38:41]
	v_mfma_f32_16x16x32_f16 v[34:37], v[130:133], v[154:157], v[34:37]
	ds_read_b128 v[130:133], v160 offset:10240
	ds_read_b128 v[146:149], v164
	ds_read_b128 v[150:153], v164 offset:2048
	ds_read_b128 v[154:157], v164 offset:4096
	s_waitcnt lgkmcnt(9)
	v_mfma_f32_16x16x32_f16 v[82:85], v[86:89], v[134:137], v[82:85]
	v_mfma_f32_16x16x32_f16 v[58:61], v[86:89], v[138:141], v[58:61]
	v_mfma_f32_16x16x32_f16 v[14:17], v[86:89], v[142:145], v[14:17]
	v_mfma_f32_16x16x32_f16 v[78:81], v[90:93], v[134:137], v[78:81]
	v_mfma_f32_16x16x32_f16 v[22:25], v[90:93], v[138:141], v[22:25]
	v_mfma_f32_16x16x32_f16 v[30:33], v[90:93], v[142:145], v[30:33]
	v_mfma_f32_16x16x32_f16 v[74:77], v[94:97], v[134:137], v[74:77]
	v_mfma_f32_16x16x32_f16 v[18:21], v[94:97], v[138:141], v[18:21]
	v_mfma_f32_16x16x32_f16 v[26:29], v[94:97], v[142:145], v[26:29]
	v_mfma_f32_16x16x32_f16 v[70:73], v[98:101], v[134:137], v[70:73]
	v_mfma_f32_16x16x32_f16 v[46:49], v[98:101], v[138:141], v[46:49]
	v_mfma_f32_16x16x32_f16 v[240:243], v[98:101], v[142:145], v[240:243]
	v_mfma_f32_16x16x32_f16 v[66:69], v[102:105], v[134:137], v[66:69]
	v_mfma_f32_16x16x32_f16 v[42:45], v[102:105], v[138:141], v[42:45]
	v_mfma_f32_16x16x32_f16 v[236:239], v[102:105], v[142:145], v[236:239]
	v_mfma_f32_16x16x32_f16 v[62:65], v[106:109], v[134:137], v[62:65]
	v_mfma_f32_16x16x32_f16 v[38:41], v[106:109], v[138:141], v[38:41]
	v_mfma_f32_16x16x32_f16 v[34:37], v[106:109], v[142:145], v[34:37]
	s_waitcnt lgkmcnt(0)
	v_mfma_f32_16x16x32_f16 v[82:85], v[110:113], v[146:149], v[82:85]
	v_mfma_f32_16x16x32_f16 v[58:61], v[110:113], v[150:153], v[58:61]
	v_mfma_f32_16x16x32_f16 v[14:17], v[110:113], v[154:157], v[14:17]
	v_mfma_f32_16x16x32_f16 v[78:81], v[114:117], v[146:149], v[78:81]
	v_mfma_f32_16x16x32_f16 v[22:25], v[114:117], v[150:153], v[22:25]
	v_mfma_f32_16x16x32_f16 v[30:33], v[114:117], v[154:157], v[30:33]
	v_mfma_f32_16x16x32_f16 v[74:77], v[118:121], v[146:149], v[74:77]
	v_mfma_f32_16x16x32_f16 v[18:21], v[118:121], v[150:153], v[18:21]
	v_mfma_f32_16x16x32_f16 v[26:29], v[118:121], v[154:157], v[26:29]
	v_mfma_f32_16x16x32_f16 v[70:73], v[122:125], v[146:149], v[70:73]
	v_mfma_f32_16x16x32_f16 v[46:49], v[122:125], v[150:153], v[46:49]
	v_mfma_f32_16x16x32_f16 v[240:243], v[122:125], v[154:157], v[240:243]
	v_mfma_f32_16x16x32_f16 v[66:69], v[126:129], v[146:149], v[66:69]
	v_mfma_f32_16x16x32_f16 v[42:45], v[126:129], v[150:153], v[42:45]
	v_mfma_f32_16x16x32_f16 v[236:239], v[126:129], v[154:157], v[236:239]
	v_mfma_f32_16x16x32_f16 v[62:65], v[130:133], v[146:149], v[62:65]
	v_mfma_f32_16x16x32_f16 v[38:41], v[130:133], v[150:153], v[38:41]
	v_mfma_f32_16x16x32_f16 v[34:37], v[130:133], v[154:157], v[34:37]
